# speedup vs baseline: 1.0038x; 1.0038x over previous
.Lattn_unit:
	s_load_dwordx4 s[4:7], s[0:1], 0x0
	s_lshr_b32 s0, s2, 2
	s_and_b32 s3, s2, 7
	s_and_b32 s0, s0, 8
	s_or_b32 s30, s0, s3
	s_lshr_b32 s18, s2, 6
	s_mov_b32 s19, 0
	s_lshl_b32 s0, s2, 5
	v_readfirstlane_b32 s16, v0
	s_and_b32 s12, s0, 0x300
	s_xor_b32 s12, s12, s91
	s_lshl_b64 s[8:9], s[18:19], 15
	s_lshl_b32 s0, s30, 11
	s_lshr_b32 s33, s16, 6
	s_or_b32 s8, s8, s0
	s_or_b32 s0, s8, s12
	s_lshl_b32 s31, s33, 5
	s_add_u32 s0, s0, s31
	s_addc_u32 s1, s9, 0
	s_lshl_b64 s[0:1], s[0:1], 7
	s_waitcnt lgkmcnt(0)
	s_add_u32 s0, s4, s0
	s_addc_u32 s1, s5, s1
	s_lshl_b64 s[10:11], s[8:9], 7
	v_bfe_u32 v190, v0, 3, 3
	s_add_u32 s10, s4, s10
	v_lshl_or_b32 v182, s33, 3, v190
	s_addc_u32 s11, s5, s11
	v_lshrrev_b32_e32 v89, 1, v182
	s_add_u32 s14, s10, 0x1000000
	v_xor_b32_e32 v4, v89, v0
	s_addc_u32 s15, s11, 0
	v_mov_b32_e32 v183, 0
	v_lshlrev_b32_e32 v4, 4, v4
	s_add_u32 s10, s10, 0x2000000
	v_lshlrev_b64 v[86:87], 7, v[182:183]
	v_and_b32_e32 v1, 7, v0
	v_and_b32_e32 v182, 0x70, v4
	v_lshrrev_b32_e32 v4, 2, v0
	s_addc_u32 s11, s11, 0
	v_lshl_add_u64 v[2:3], s[14:15], 0, v[86:87]
	v_bitop3_b32 v4, v4, v1, 4 bitop3:0x6c
	v_lshl_add_u64 v[186:187], v[2:3], 0, v[182:183]
	v_lshl_add_u64 v[2:3], s[10:11], 0, v[86:87]
	v_lshlrev_b32_e32 v182, 4, v4
	s_lshl_b32 s36, s33, 10
	s_mov_b32 s13, m0
	s_mov_b32 m0, s36
	s_nop 0
	global_load_lds_dwordx4 v[186:187], off
	s_mov_b32 m0, s13
	s_mov_b64 s[20:21], 0x2000
	v_and_b32_e32 v191, 31, v0
	v_lshl_add_u64 v[194:195], v[2:3], 0, v[182:183]
	s_add_i32 s35, s36, 0x6000
	s_mov_b32 s13, m0
	s_mov_b32 m0, s35
	s_nop 0
	global_load_lds_dwordx4 v[194:195], off
	s_mov_b32 m0, s13
	v_lshl_add_u64 v[2:3], v[186:187], 0, s[20:21]
	v_bfe_u32 v88, v0, 5, 1
	s_add_i32 s37, s36, 0x2000
	s_mov_b32 s13, m0
	s_mov_b32 m0, s37
	s_nop 0
	global_load_lds_dwordx4 v[2:3], off
	s_mov_b32 m0, s13
	v_lshlrev_b32_e32 v2, 6, v191
	v_lshl_or_b32 v192, v88, 3, v2
	v_lshlrev_b32_e32 v14, 1, v192
	global_load_dwordx4 v[154:157], v14, s[0:1]
	global_load_dwordx4 v[146:149], v14, s[0:1] offset:32
	global_load_dwordx4 v[138:141], v14, s[0:1] offset:64
	global_load_dwordx4 v[134:137], v14, s[0:1] offset:96
	v_lshrrev_b32_e32 v18, 1, v0
	s_mov_b64 s[22:23], 0x4000
	v_mov_b32_e32 v2, v183
	v_mov_b32_e32 v3, v183
	v_mov_b32_e32 v4, v183
	v_mov_b32_e32 v5, v183
	v_mov_b32_e32 v6, v183
	v_mov_b32_e32 v7, v183
	v_mov_b32_e32 v8, v183
	v_mov_b32_e32 v9, v183
	v_mov_b32_e32 v10, v183
	v_mov_b32_e32 v11, v183
	v_mov_b32_e32 v12, v183
	v_mov_b32_e32 v13, v183
	v_mov_b32_e32 v14, v183
	v_mov_b32_e32 v15, v183
	v_mov_b32_e32 v16, v183
	v_mov_b32_e32 v17, v183
	v_lshlrev_b32_e32 v38, 7, v191
	v_bitop3_b32 v18, v88, v18, 7 bitop3:0x78
	v_lshl_or_b32 v211, v18, 4, v38
	v_lshl_add_u64 v[18:19], v[186:187], 0, s[22:23]
	s_add_i32 s0, s36, 0x4000
	s_mov_b32 s1, m0
	s_mov_b32 m0, s0
	s_nop 0
	global_load_lds_dwordx4 v[18:19], off
	s_mov_b32 m0, s1
	s_waitcnt vmcnt(3) lgkmcnt(0)
	s_barrier
	ds_read_b128 v[34:37], v211
	v_bfe_u32 v39, v0, 1, 3
	v_bitop3_b32 v40, v88, v39, 2 bitop3:0x36
	v_lshl_or_b32 v210, v40, 4, v38
	v_bitop3_b32 v40, v88, v39, 4 bitop3:0x36
	v_lshl_or_b32 v209, v40, 4, v38
	v_bitop3_b32 v39, v88, v39, 6 bitop3:0x36
	v_lshl_or_b32 v208, v39, 4, v38
	v_lshlrev_b32_e32 v201, 9, v88
	s_and_b32 s0, s16, 0x3fffffc0
	s_mov_b64 s[24:25], 0x6000
	s_lshl_b32 s38, s0, 2
	s_add_i32 s34, s36, 0x8000
	s_lshl_b32 s2, s2, 16
	s_lshl_b32 s3, s3, 18
	s_waitcnt vmcnt(3) lgkmcnt(0)
	v_mfma_f32_32x32x16_f16 v[18:33], v[34:37], v[154:157], v[2:17]
	ds_read_b128 v[34:37], v211 offset:4096
	s_and_b32 s2, s2, 0x200000
	s_lshl_b64 s[16:17], s[18:19], 22
	s_or_b32 s2, s2, s3
	s_or_b32 s16, s16, s2
	s_mov_b64 s[2:3], 0x1002000
	v_and_b32_e32 v90, 63, v0
	s_waitcnt lgkmcnt(0)
	v_mfma_f32_32x32x16_f16 v[2:17], v[34:37], v[154:157], v[2:17]
	ds_read_b128 v[34:37], v210
	s_mov_b32 s13, s19
	s_movk_i32 s42, 0x2000
	s_movk_i32 s39, 0x4000
	v_lshl_or_b32 v204, v191, 2, s38
	v_lshlrev_b32_e32 v212, 4, v88
	s_mov_b32 s40, -1
	s_waitcnt vmcnt(2) lgkmcnt(0)
	v_mfma_f32_32x32x16_f16 v[18:33], v[34:37], v[146:149], v[18:33]
	ds_read_b128 v[34:37], v210 offset:4096
	s_mov_b32 s41, 0x41000000
	s_mov_b32 s26, s19
	s_waitcnt lgkmcnt(0)
	v_mfma_f32_32x32x16_f16 v[2:17], v[34:37], v[146:149], v[2:17]
	ds_read_b128 v[34:37], v209
	s_waitcnt vmcnt(1) lgkmcnt(0)
	v_mfma_f32_32x32x16_f16 v[18:33], v[34:37], v[138:141], v[18:33]
	ds_read_b128 v[34:37], v209 offset:4096
	ds_read_b128 v[38:41], v208 offset:4096
	ds_read_b128 v[42:45], v208
	s_waitcnt lgkmcnt(2)
	v_mfma_f32_32x32x16_f16 v[2:17], v[34:37], v[138:141], v[2:17]
	v_lshlrev_b32_e32 v34, 5, v0
	v_lshlrev_b32_e32 v35, 1, v0
	v_lshlrev_b32_e32 v36, 3, v0
	v_and_b32_e32 v34, 0x180, v34
	v_and_b32_e32 v193, 24, v36
	v_and_or_b32 v34, v35, 32, v34
	v_or3_b32 v203, v34, v193, v201
	s_waitcnt vmcnt(0) lgkmcnt(0)
	v_mfma_f32_32x32x16_f16 v[18:33], v[42:45], v[134:137], v[18:33]
	v_and_b32_e32 v200, 64, v36
	v_bitop3_b32 v202, v36, 64, v36 bitop3:0xc
	v_or_b32_e32 v206, v203, v200
	v_or_b32_e32 v207, v203, v202
	v_mfma_f32_32x32x16_f16 v[2:17], v[38:41], v[134:137], v[2:17]
	s_nop 15
	s_nop 7
	s_nop 0
	v_max3_f32 v34, v18, v19, v2
	v_max3_f32 v35, v20, v21, v3
	s_nop 0
	v_max3_f32 v34, v34, v4, v5
	v_max3_f32 v35, v35, v24, v25
	s_nop 0
	v_max3_f32 v34, v34, v22, v23
	v_max3_f32 v35, v35, v8, v9
	s_nop 0
	v_max3_f32 v34, v34, v6, v7
	v_max3_f32 v35, v35, v28, v29
	s_nop 0
	v_max3_f32 v34, v34, v26, v27
	v_max3_f32 v35, v35, v12, v13
	s_nop 0
	v_max3_f32 v34, v34, v10, v11
	v_max3_f32 v35, v35, v32, v33
	s_nop 0
	v_max3_f32 v34, v34, v30, v31
	v_max3_f32 v35, v35, v16, v17
	s_nop 0
	v_max3_f32 v34, v34, v14, v15
	s_nop 0
	v_max_f32_e32 v34, v34, v35
	s_nop 0
	v_mov_b32_e32 v35, v34
	s_nop 1
	v_permlane32_swap_b32_e32 v34, v35
	v_max_f32_e32 v34, v34, v35
	s_nop 0
	v_add_f32_e32 v205, v183, v34
	v_sub_f32_e32 v18, v18, v34
	v_sub_f32_e32 v2, v2, v34
	v_sub_f32_e32 v19, v19, v34
	v_sub_f32_e32 v3, v3, v34
	v_sub_f32_e32 v20, v20, v34
	v_sub_f32_e32 v4, v4, v34
	v_sub_f32_e32 v21, v21, v34
	v_sub_f32_e32 v5, v5, v34
	v_sub_f32_e32 v22, v22, v34
	v_sub_f32_e32 v6, v6, v34
	v_sub_f32_e32 v23, v23, v34
	v_sub_f32_e32 v7, v7, v34
	v_sub_f32_e32 v24, v24, v34
	v_sub_f32_e32 v8, v8, v34
	v_sub_f32_e32 v25, v25, v34
	v_sub_f32_e32 v9, v9, v34
	v_sub_f32_e32 v26, v26, v34
	v_sub_f32_e32 v10, v10, v34
	v_sub_f32_e32 v27, v27, v34
	v_sub_f32_e32 v11, v11, v34
	v_sub_f32_e32 v28, v28, v34
	v_sub_f32_e32 v12, v12, v34
	v_sub_f32_e32 v29, v29, v34
	v_sub_f32_e32 v13, v13, v34
	v_sub_f32_e32 v30, v30, v34
	v_sub_f32_e32 v14, v14, v34
	v_sub_f32_e32 v31, v31, v34
	v_sub_f32_e32 v15, v15, v34
	v_sub_f32_e32 v32, v32, v34
	v_sub_f32_e32 v16, v16, v34
	v_sub_f32_e32 v33, v33, v34
	v_sub_f32_e32 v17, v17, v34
	s_nop 0
	v_xor_b32_e32 v34, 0x80000000, v205
	v_mov_b32_e32 v35, v34
	v_mov_b32_e32 v36, v34
	v_mov_b32_e32 v37, v34
	v_mov_b32_e32 v38, v34
	v_mov_b32_e32 v39, v34
	v_mov_b32_e32 v40, v34
	v_mov_b32_e32 v41, v34
	v_mov_b32_e32 v42, v34
	v_mov_b32_e32 v43, v34
	v_mov_b32_e32 v44, v34
	v_mov_b32_e32 v45, v34
	v_mov_b32_e32 v46, v34
	v_mov_b32_e32 v47, v34
	v_mov_b32_e32 v48, v34
	v_mov_b32_e32 v49, v34
	s_waitcnt vmcnt(0) lgkmcnt(0)
	s_barrier
	v_exp_f32_e32 v50, v2
	v_exp_f32_e32 v51, v3
	v_lshl_add_u64 v[2:3], v[186:187], 0, s[24:25]
	s_mov_b32 s0, m0
	s_mov_b32 m0, s36
	s_nop 0
	global_load_lds_dwordx4 v[2:3], off
	s_mov_b32 m0, s0
	v_lshl_add_u64 v[2:3], v[194:195], 0, s[20:21]
	s_mov_b32 s0, m0
	s_mov_b32 m0, s34
	s_nop 0
	global_load_lds_dwordx4 v[2:3], off
	s_mov_b32 m0, s0
	ds_read_b128 v[82:85], v211 offset:8192
	ds_read_b128 v[170:173], v211 offset:12288
	ds_read_b128 v[166:169], v210 offset:8192
	ds_read_b128 v[162:165], v210 offset:12288
	ds_read_b128 v[126:129], v209 offset:8192
	ds_read_b128 v[122:125], v209 offset:12288
	ds_read_b128 v[118:121], v208 offset:8192
	ds_read_b128 v[114:117], v208 offset:12288
	v_exp_f32_e32 v52, v4
	v_lshl_add_u64 v[2:3], s[16:17], 0, v[86:87]
	v_bitop3_b32 v4, v89, 7, v0 bitop3:0x48
	v_exp_f32_e32 v66, v18
	v_exp_f32_e32 v67, v19
	v_exp_f32_e32 v68, v20
	v_exp_f32_e32 v69, v21
	v_exp_f32_e32 v70, v22
	v_exp_f32_e32 v71, v23
	v_exp_f32_e32 v72, v24
	v_exp_f32_e32 v73, v25
	v_exp_f32_e32 v74, v26
	v_exp_f32_e32 v75, v27
	v_exp_f32_e32 v76, v28
	v_exp_f32_e32 v77, v29
	v_exp_f32_e32 v78, v30
	v_exp_f32_e32 v79, v31
	v_exp_f32_e32 v80, v32
	v_exp_f32_e32 v81, v33
	v_exp_f32_e32 v53, v5
	v_exp_f32_e32 v54, v6
	v_exp_f32_e32 v55, v7
	v_exp_f32_e32 v56, v8
	v_exp_f32_e32 v57, v9
	v_exp_f32_e32 v58, v10
	v_exp_f32_e32 v59, v11
	v_exp_f32_e32 v60, v12
	v_exp_f32_e32 v61, v13
	v_exp_f32_e32 v62, v14
	v_exp_f32_e32 v63, v15
	v_exp_f32_e32 v64, v16
	v_exp_f32_e32 v65, v17
	v_lshl_or_b32 v4, v4, 4, v2
	v_mov_b32_e32 v5, v3
	s_waitcnt vmcnt(2) lgkmcnt(0)
	s_barrier
	v_lshl_add_u64 v[4:5], s[4:5], 0, v[4:5]
	v_or_b32_e32 v2, v2, v182
	v_lshl_add_u64 v[188:189], v[4:5], 0, s[2:3]
	v_lshl_add_u64 v[2:3], s[4:5], 0, v[2:3]
	s_mov_b64 s[2:3], 0x2002000
	v_cmp_gt_u32_e64 s[0:1], 32, v90
	v_lshl_add_u64 v[196:197], v[2:3], 0, s[2:3]
	s_mov_b64 s[2:3], 0x8000
	v_mov_b32_e32 v2, v183
	v_mov_b32_e32 v3, v183
	v_mov_b32_e32 v4, v183
	v_mov_b32_e32 v5, v183
	v_mov_b32_e32 v6, v183
	v_mov_b32_e32 v7, v183
	v_mov_b32_e32 v8, v183
	v_mov_b32_e32 v9, v183
	v_mov_b32_e32 v10, v183
	v_mov_b32_e32 v11, v183
	v_mov_b32_e32 v12, v183
	v_mov_b32_e32 v13, v183
	v_mov_b32_e32 v14, v183
	v_mov_b32_e32 v15, v183
	v_mov_b32_e32 v16, v183
	v_mov_b32_e32 v17, v183
	v_mov_b32_e32 v18, v183
	v_mov_b32_e32 v19, v183
	v_mov_b32_e32 v20, v183
	v_mov_b32_e32 v21, v183
	v_mov_b32_e32 v22, v183
	v_mov_b32_e32 v23, v183
	v_mov_b32_e32 v24, v183
	v_mov_b32_e32 v25, v183
	v_mov_b32_e32 v26, v183
	v_mov_b32_e32 v27, v183
	v_mov_b32_e32 v28, v183
	v_mov_b32_e32 v29, v183
	v_mov_b32_e32 v30, v183
	v_mov_b32_e32 v31, v183
	v_mov_b32_e32 v32, v183
	v_mov_b32_e32 v33, v183
	v_subrev_u32_e32 v221, s14, v186
	v_subrev_u32_e32 v222, s10, v194
	s_add_u32 s50, s14, 0x8000
	s_addc_u32 s51, s15, 0
	s_add_u32 s52, s10, 0x4000
	s_addc_u32 s53, s11, 0
.Lu0_1:
	ds_read_b64_tr_b16 v[178:179], v206 offset:24576
	ds_read_b64_tr_b16 v[180:181], v206 offset:25600
	s_waitcnt lgkmcnt(9)
	v_mfma_f32_32x32x16_f16 v[98:113], v[82:85], v[154:157], v[34:49]
	v_add_f32_e32 v86, v66, v67
	v_add_f32_e32 v86, v68, v86
	v_add_f32_e32 v86, v69, v86
	v_add_f32_e32 v86, v70, v86
	v_add_f32_e32 v86, v71, v86
	v_cvt_pk_f16_f32 v158, v66, v67
	v_cvt_pk_f16_f32 v159, v68, v69
	ds_read_b64_tr_b16 v[174:175], v207 offset:24576
	ds_read_b64_tr_b16 v[176:177], v207 offset:25600
	v_add_f32_e32 v66, v72, v86
	s_waitcnt lgkmcnt(10)
	v_mfma_f32_32x32x16_f16 v[82:97], v[170:173], v[154:157], v[34:49]
	v_add_f32_e32 v66, v73, v66
	v_add_f32_e32 v66, v74, v66
	v_add_f32_e32 v66, v75, v66
	v_cvt_pk_f16_f32 v160, v70, v71
	v_cvt_pk_f16_f32 v161, v72, v73
	ds_read_b64_tr_b16 v[170:171], v206 offset:26624
	ds_read_b64_tr_b16 v[172:173], v206 offset:27648
	s_waitcnt lgkmcnt(11)
	v_mfma_f32_32x32x16_f16 v[98:113], v[166:169], v[146:149], v[98:113]
	v_add_f32_e32 v66, v76, v66
	v_add_f32_e32 v66, v77, v66
	v_add_f32_e32 v66, v78, v66
	v_add_f32_e32 v66, v79, v66
	v_cvt_pk_f16_f32 v150, v74, v75
	v_cvt_pk_f16_f32 v151, v76, v77
	ds_read_b64_tr_b16 v[74:75], v207 offset:26624
	ds_read_b64_tr_b16 v[76:77], v207 offset:27648
	s_waitcnt lgkmcnt(12)
	v_mfma_f32_32x32x16_f16 v[82:97], v[162:165], v[146:149], v[82:97]
	v_add_f32_e32 v66, v80, v66
	v_add_f32_e32 v66, v81, v66
	v_add_f32_e32 v66, v50, v66
	v_add_f32_e32 v66, v51, v66
	v_cvt_pk_f16_f32 v152, v78, v79
	v_cvt_pk_f16_f32 v153, v80, v81
	ds_read_b64_tr_b16 v[70:71], v206 offset:28672
	ds_read_b64_tr_b16 v[72:73], v206 offset:29696
	s_waitcnt lgkmcnt(13)
	v_mfma_f32_32x32x16_f16 v[98:113], v[126:129], v[138:141], v[98:113]
	v_add_f32_e32 v66, v52, v66
	v_add_f32_e32 v66, v53, v66
	v_add_f32_e32 v66, v54, v66
	v_add_f32_e32 v78, v55, v66
	v_cvt_pk_f16_f32 v142, v50, v51
	v_cvt_pk_f16_f32 v143, v52, v53
	ds_read_b64_tr_b16 v[66:67], v207 offset:28672
	ds_read_b64_tr_b16 v[68:69], v207 offset:29696
	s_waitcnt lgkmcnt(14)
	v_mfma_f32_32x32x16_f16 v[82:97], v[122:125], v[138:141], v[82:97]
	v_add_f32_e32 v50, v56, v78
	v_add_f32_e32 v50, v57, v50
	v_add_f32_e32 v50, v58, v50
	v_add_f32_e32 v50, v59, v50
	v_cvt_pk_f16_f32 v144, v54, v55
	v_cvt_pk_f16_f32 v145, v56, v57
	ds_read_b64_tr_b16 v[54:55], v206 offset:30720
	ds_read_b64_tr_b16 v[56:57], v206 offset:31744
	s_waitcnt lgkmcnt(14)
	v_mfma_f32_32x32x16_f16 v[98:113], v[118:121], v[134:137], v[98:113]
	v_add_f32_e32 v50, v60, v50
	v_add_f32_e32 v50, v61, v50
	v_add_f32_e32 v50, v62, v50
	v_add_f32_e32 v78, v63, v50
	v_cvt_pk_f16_f32 v130, v58, v59
	v_cvt_pk_f16_f32 v131, v60, v61
	ds_read_b64_tr_b16 v[50:51], v207 offset:30720
	ds_read_b64_tr_b16 v[52:53], v207 offset:31744
	v_mfma_f32_32x32x16_f16 v[82:97], v[114:117], v[134:137], v[82:97]
	v_add_f32_e32 v58, v64, v78
	v_add_f32_e32 v60, v65, v58
	v_cvt_pk_f16_f32 v132, v62, v63
	v_cvt_pk_f16_f32 v133, v64, v65
	s_add_i32 s26, s42, s36
	s_mov_b32 m0, s26
	s_nop 0
	global_load_lds_dwordx4 v221, s[50:51]
	s_add_i32 s26, s39, s35
	s_mov_b32 m0, s26
	s_nop 0
	global_load_lds_dwordx4 v222, s[52:53]
	v_max_f32_e32 v58, v98, v99
	v_max3_f32 v59, v100, v101, v83
	v_max3_f32 v58, v58, v82, v84
	v_max3_f32 v58, v58, v85, v102
	v_max3_f32 v59, v59, v104, v105
	v_max3_f32 v58, v58, v103, v86
	v_max3_f32 v59, v59, v88, v89
	v_max3_f32 v58, v58, v87, v106
	v_max3_f32 v59, v59, v108, v109
	v_max3_f32 v58, v58, v107, v90
	v_max3_f32 v59, v59, v92, v93
	v_max3_f32 v58, v58, v91, v110
	v_max3_f32 v59, v59, v112, v113
	v_max3_f32 v58, v58, v111, v94
	v_max3_f32 v59, v59, v96, v97
	v_max3_f32 v58, v58, v95, v59
	v_mov_b32_e32 v59, v58
	v_add_f32_e32 v198, v183, v60
	s_nop 0
	v_permlane32_swap_b32_e32 v58, v59
	v_max_f32_e32 v58, v58, v59
	v_cmp_lt_f32_e32 vcc, s41, v58
	s_cmp_lg_u64 vcc, 0
	s_cselect_b64 s[26:27], -1, 0
	s_cbranch_vccnz .Lu0_9

.Lu0_4:
	s_add_i32 s26, s39, 0x2000
	s_cmpk_lg_i32 s39, 0x4000
	s_cselect_b32 s43, s26, 0
	ds_read_b64_tr_b16 v[126:127], v206 offset:32768
	ds_read_b64_tr_b16 v[128:129], v206 offset:33792
	s_waitcnt lgkmcnt(9)
	v_mfma_f32_32x32x16_f16 v[66:81], v[58:61], v[154:157], v[34:49]
	v_add_f32_e32 v50, v98, v99
	v_add_f32_e32 v50, v100, v50
	v_add_f32_e32 v50, v101, v50
	v_add_f32_e32 v50, v102, v50
	v_add_f32_e32 v50, v103, v50
	v_cvt_pk_f16_f32 v158, v98, v99
	v_cvt_pk_f16_f32 v159, v100, v101
	ds_read_b64_tr_b16 v[122:123], v207 offset:32768
	ds_read_b64_tr_b16 v[124:125], v207 offset:33792
	v_add_f32_e32 v50, v104, v50
	v_add_f32_e32 v50, v105, v50
	v_add_f32_e32 v50, v106, v50
	v_add_f32_e32 v98, v107, v50
	s_waitcnt lgkmcnt(10)
	v_mfma_f32_32x32x16_f16 v[50:65], v[114:117], v[154:157], v[34:49]
	v_cvt_pk_f16_f32 v160, v102, v103
	v_cvt_pk_f16_f32 v161, v104, v105
	ds_read_b64_tr_b16 v[118:119], v206 offset:34816
	ds_read_b64_tr_b16 v[120:121], v206 offset:35840
	s_waitcnt lgkmcnt(11)
	v_mfma_f32_32x32x16_f16 v[66:81], v[182:185], v[146:149], v[66:81]
	v_add_f32_e32 v98, v108, v98
	v_add_f32_e32 v98, v109, v98
	v_add_f32_e32 v98, v110, v98
	v_add_f32_e32 v98, v111, v98
	v_cvt_pk_f16_f32 v150, v106, v107
	v_cvt_pk_f16_f32 v151, v108, v109
	ds_read_b64_tr_b16 v[114:115], v207 offset:34816
	ds_read_b64_tr_b16 v[116:117], v207 offset:35840
	s_waitcnt lgkmcnt(12)
	v_mfma_f32_32x32x16_f16 v[50:65], v[174:177], v[146:149], v[50:65]
	v_add_f32_e32 v98, v112, v98
	v_add_f32_e32 v98, v113, v98
	v_add_f32_e32 v98, v82, v98
	v_add_f32_e32 v98, v83, v98
	v_cvt_pk_f16_f32 v152, v110, v111
	v_cvt_pk_f16_f32 v153, v112, v113
	ds_read_b64_tr_b16 v[106:107], v206 offset:36864
	ds_read_b64_tr_b16 v[108:109], v206 offset:37888
	s_waitcnt lgkmcnt(13)
	v_mfma_f32_32x32x16_f16 v[66:81], v[178:181], v[138:141], v[66:81]
	v_add_f32_e32 v98, v84, v98
	v_add_f32_e32 v98, v85, v98
	v_add_f32_e32 v98, v86, v98
	v_add_f32_e32 v98, v87, v98
	v_cvt_pk_f16_f32 v142, v82, v83
	v_cvt_pk_f16_f32 v143, v84, v85
	ds_read_b64_tr_b16 v[102:103], v207 offset:36864
	ds_read_b64_tr_b16 v[104:105], v207 offset:37888
	s_waitcnt lgkmcnt(14)
	v_mfma_f32_32x32x16_f16 v[50:65], v[166:169], v[138:141], v[50:65]
	v_add_f32_e32 v82, v88, v98
	v_add_f32_e32 v82, v89, v82
	v_add_f32_e32 v82, v90, v82
	v_add_f32_e32 v82, v91, v82
	v_cvt_pk_f16_f32 v144, v86, v87
	v_cvt_pk_f16_f32 v145, v88, v89
	ds_read_b64_tr_b16 v[98:99], v206 offset:38912
	ds_read_b64_tr_b16 v[100:101], v206 offset:39936
	s_waitcnt lgkmcnt(14)
	v_mfma_f32_32x32x16_f16 v[66:81], v[170:173], v[134:137], v[66:81]
	v_add_f32_e32 v82, v92, v82
	v_add_f32_e32 v82, v93, v82
	v_add_f32_e32 v82, v94, v82
	v_add_f32_e32 v82, v95, v82
	v_cvt_pk_f16_f32 v130, v90, v91
	v_cvt_pk_f16_f32 v131, v92, v93
	ds_read_b64_tr_b16 v[86:87], v207 offset:38912
	ds_read_b64_tr_b16 v[88:89], v207 offset:39936
	v_mfma_f32_32x32x16_f16 v[50:65], v[162:165], v[134:137], v[50:65]
	v_add_f32_e32 v82, v96, v82
	v_add_f32_e32 v84, v97, v82
	v_cvt_pk_f16_f32 v132, v94, v95
	v_cvt_pk_f16_f32 v133, v96, v97
	s_add_u32 s54, s50, 0x2000
	s_addc_u32 s55, s51, 0
	s_add_i32 s26, s39, s36
	s_mov_b32 m0, s26
	s_nop 0
	global_load_lds_dwordx4 v221, s[54:55]
	v_max_f32_e32 v82, v66, v67
	s_nop 1
	v_max3_f32 v83, v68, v69, v51
	v_max3_f32 v82, v82, v50, v52
	v_max3_f32 v82, v82, v53, v70
	v_max3_f32 v83, v83, v72, v73
	v_max3_f32 v82, v82, v71, v54
	v_max3_f32 v83, v83, v56, v57
	v_max3_f32 v82, v82, v55, v74
	v_max3_f32 v83, v83, v76, v77
	v_max3_f32 v82, v82, v75, v58
	v_max3_f32 v83, v83, v60, v61
	v_max3_f32 v82, v82, v59, v78
	v_max3_f32 v83, v83, v80, v81
	v_max3_f32 v82, v82, v79, v62
	v_max3_f32 v83, v83, v64, v65
	v_max3_f32 v82, v82, v63, v83
	v_mov_b32_e32 v83, v82
	v_add_f32_e32 v183, v198, v84
	s_nop 0
	v_permlane32_swap_b32_e32 v82, v83
	v_max_f32_e32 v82, v82, v83
	s_add_u32 s54, s52, 0x2000
	s_addc_u32 s55, s53, 0
	s_add_i32 s26, s43, s35
	s_mov_b32 m0, s26
	s_nop 0
	global_load_lds_dwordx4 v222, s[54:55]
	v_cmp_lt_f32_e32 vcc, s41, v82
	s_cmp_lg_u64 vcc, 0
	s_cselect_b64 s[26:27], -1, 0
	s_cbranch_vccnz .Lu0_12

.Lu0_7:
	s_add_u32 s50, s50, 0x4000
	s_addc_u32 s51, s51, 0
	s_add_u32 s52, s52, 0x4000
	s_addc_u32 s53, s53, 0
	s_add_i32 s26, s43, 0x2000
	s_cmpk_lg_i32 s43, 0x4000
	s_cselect_b32 s27, s26, 0
	s_add_i32 s40, s40, 2
	s_cmp_lt_u32 s40, 25
	s_cbranch_scc0 .LBB2_15
	s_mov_b32 s26, s39
	s_mov_b32 s42, s43
	s_mov_b32 s39, s27
	s_branch .Lu1_1
.Lu1_1:
	ds_read_b64_tr_b16 v[178:179], v206 offset:40960
	ds_read_b64_tr_b16 v[180:181], v206 offset:41984
	s_waitcnt lgkmcnt(9)
	v_mfma_f32_32x32x16_f16 v[98:113], v[82:85], v[154:157], v[34:49]
	v_add_f32_e32 v86, v66, v67
	v_add_f32_e32 v86, v68, v86
	v_add_f32_e32 v86, v69, v86
	v_add_f32_e32 v86, v70, v86
	v_add_f32_e32 v86, v71, v86
	v_cvt_pk_f16_f32 v158, v66, v67
	v_cvt_pk_f16_f32 v159, v68, v69
	ds_read_b64_tr_b16 v[174:175], v207 offset:40960
	ds_read_b64_tr_b16 v[176:177], v207 offset:41984
	v_add_f32_e32 v66, v72, v86
	s_waitcnt lgkmcnt(10)
	v_mfma_f32_32x32x16_f16 v[82:97], v[170:173], v[154:157], v[34:49]
	v_add_f32_e32 v66, v73, v66
	v_add_f32_e32 v66, v74, v66
	v_add_f32_e32 v66, v75, v66
	v_cvt_pk_f16_f32 v160, v70, v71
	v_cvt_pk_f16_f32 v161, v72, v73
	ds_read_b64_tr_b16 v[170:171], v206 offset:43008
	ds_read_b64_tr_b16 v[172:173], v206 offset:44032
	s_waitcnt lgkmcnt(11)
	v_mfma_f32_32x32x16_f16 v[98:113], v[166:169], v[146:149], v[98:113]
	v_add_f32_e32 v66, v76, v66
	v_add_f32_e32 v66, v77, v66
	v_add_f32_e32 v66, v78, v66
	v_add_f32_e32 v66, v79, v66
	v_cvt_pk_f16_f32 v150, v74, v75
	v_cvt_pk_f16_f32 v151, v76, v77
	ds_read_b64_tr_b16 v[74:75], v207 offset:43008
	ds_read_b64_tr_b16 v[76:77], v207 offset:44032
	s_waitcnt lgkmcnt(12)
	v_mfma_f32_32x32x16_f16 v[82:97], v[162:165], v[146:149], v[82:97]
	v_add_f32_e32 v66, v80, v66
	v_add_f32_e32 v66, v81, v66
	v_add_f32_e32 v66, v50, v66
	v_add_f32_e32 v66, v51, v66
	v_cvt_pk_f16_f32 v152, v78, v79
	v_cvt_pk_f16_f32 v153, v80, v81
	ds_read_b64_tr_b16 v[70:71], v206 offset:45056
	ds_read_b64_tr_b16 v[72:73], v206 offset:46080
	s_waitcnt lgkmcnt(13)
	v_mfma_f32_32x32x16_f16 v[98:113], v[126:129], v[138:141], v[98:113]
	v_add_f32_e32 v66, v52, v66
	v_add_f32_e32 v66, v53, v66
	v_add_f32_e32 v66, v54, v66
	v_add_f32_e32 v78, v55, v66
	v_cvt_pk_f16_f32 v142, v50, v51
	v_cvt_pk_f16_f32 v143, v52, v53
	ds_read_b64_tr_b16 v[66:67], v207 offset:45056
	ds_read_b64_tr_b16 v[68:69], v207 offset:46080
	s_waitcnt lgkmcnt(14)
	v_mfma_f32_32x32x16_f16 v[82:97], v[122:125], v[138:141], v[82:97]
	v_add_f32_e32 v50, v56, v78
	v_add_f32_e32 v50, v57, v50
	v_add_f32_e32 v50, v58, v50
	v_add_f32_e32 v50, v59, v50
	v_cvt_pk_f16_f32 v144, v54, v55
	v_cvt_pk_f16_f32 v145, v56, v57
	ds_read_b64_tr_b16 v[54:55], v206 offset:47104
	ds_read_b64_tr_b16 v[56:57], v206 offset:48128
	s_waitcnt lgkmcnt(14)
	v_mfma_f32_32x32x16_f16 v[98:113], v[118:121], v[134:137], v[98:113]
	v_add_f32_e32 v50, v60, v50
	v_add_f32_e32 v50, v61, v50
	v_add_f32_e32 v50, v62, v50
	v_add_f32_e32 v78, v63, v50
	v_cvt_pk_f16_f32 v130, v58, v59
	v_cvt_pk_f16_f32 v131, v60, v61
	ds_read_b64_tr_b16 v[50:51], v207 offset:47104
	ds_read_b64_tr_b16 v[52:53], v207 offset:48128
	v_mfma_f32_32x32x16_f16 v[82:97], v[114:117], v[134:137], v[82:97]
	v_add_f32_e32 v58, v64, v78
	v_add_f32_e32 v60, v65, v58
	v_cvt_pk_f16_f32 v132, v62, v63
	v_cvt_pk_f16_f32 v133, v64, v65
	s_add_i32 s26, s42, s36
	s_mov_b32 m0, s26
	s_nop 0
	global_load_lds_dwordx4 v221, s[50:51]
	s_add_i32 s26, s39, s35
	s_mov_b32 m0, s26
	s_nop 0
	global_load_lds_dwordx4 v222, s[52:53]
	v_max_f32_e32 v58, v98, v99
	v_max3_f32 v59, v100, v101, v83
	v_max3_f32 v58, v58, v82, v84
	v_max3_f32 v58, v58, v85, v102
	v_max3_f32 v59, v59, v104, v105
	v_max3_f32 v58, v58, v103, v86
	v_max3_f32 v59, v59, v88, v89
	v_max3_f32 v58, v58, v87, v106
	v_max3_f32 v59, v59, v108, v109
	v_max3_f32 v58, v58, v107, v90
	v_max3_f32 v59, v59, v92, v93
	v_max3_f32 v58, v58, v91, v110
	v_max3_f32 v59, v59, v112, v113
	v_max3_f32 v58, v58, v111, v94
	v_max3_f32 v59, v59, v96, v97
	v_max3_f32 v58, v58, v95, v59
	v_mov_b32_e32 v59, v58
	v_add_f32_e32 v198, v183, v60
	s_nop 0
	v_permlane32_swap_b32_e32 v58, v59
	v_max_f32_e32 v58, v58, v59
	v_cmp_lt_f32_e32 vcc, s41, v58
	s_cmp_lg_u64 vcc, 0
	s_cselect_b64 s[26:27], -1, 0
	s_cbranch_vccnz .Lu1_9

.Lu1_4:
	s_add_i32 s26, s39, 0x2000
	s_cmpk_lg_i32 s39, 0x4000
	s_cselect_b32 s43, s26, 0
	ds_read_b64_tr_b16 v[126:127], v206 offset:24576
	ds_read_b64_tr_b16 v[128:129], v206 offset:25600
	s_waitcnt lgkmcnt(9)
	v_mfma_f32_32x32x16_f16 v[66:81], v[58:61], v[154:157], v[34:49]
	v_add_f32_e32 v50, v98, v99
	v_add_f32_e32 v50, v100, v50
	v_add_f32_e32 v50, v101, v50
	v_add_f32_e32 v50, v102, v50
	v_add_f32_e32 v50, v103, v50
	v_cvt_pk_f16_f32 v158, v98, v99
	v_cvt_pk_f16_f32 v159, v100, v101
	ds_read_b64_tr_b16 v[122:123], v207 offset:24576
	ds_read_b64_tr_b16 v[124:125], v207 offset:25600
	v_add_f32_e32 v50, v104, v50
	v_add_f32_e32 v50, v105, v50
	v_add_f32_e32 v50, v106, v50
	v_add_f32_e32 v98, v107, v50
	s_waitcnt lgkmcnt(10)
	v_mfma_f32_32x32x16_f16 v[50:65], v[114:117], v[154:157], v[34:49]
	v_cvt_pk_f16_f32 v160, v102, v103
	v_cvt_pk_f16_f32 v161, v104, v105
	ds_read_b64_tr_b16 v[118:119], v206 offset:26624
	ds_read_b64_tr_b16 v[120:121], v206 offset:27648
	s_waitcnt lgkmcnt(11)
	v_mfma_f32_32x32x16_f16 v[66:81], v[182:185], v[146:149], v[66:81]
	v_add_f32_e32 v98, v108, v98
	v_add_f32_e32 v98, v109, v98
	v_add_f32_e32 v98, v110, v98
	v_add_f32_e32 v98, v111, v98
	v_cvt_pk_f16_f32 v150, v106, v107
	v_cvt_pk_f16_f32 v151, v108, v109
	ds_read_b64_tr_b16 v[114:115], v207 offset:26624
	ds_read_b64_tr_b16 v[116:117], v207 offset:27648
	s_waitcnt lgkmcnt(12)
	v_mfma_f32_32x32x16_f16 v[50:65], v[174:177], v[146:149], v[50:65]
	v_add_f32_e32 v98, v112, v98
	v_add_f32_e32 v98, v113, v98
	v_add_f32_e32 v98, v82, v98
	v_add_f32_e32 v98, v83, v98
	v_cvt_pk_f16_f32 v152, v110, v111
	v_cvt_pk_f16_f32 v153, v112, v113
	ds_read_b64_tr_b16 v[106:107], v206 offset:28672
	ds_read_b64_tr_b16 v[108:109], v206 offset:29696
	s_waitcnt lgkmcnt(13)
	v_mfma_f32_32x32x16_f16 v[66:81], v[178:181], v[138:141], v[66:81]
	v_add_f32_e32 v98, v84, v98
	v_add_f32_e32 v98, v85, v98
	v_add_f32_e32 v98, v86, v98
	v_add_f32_e32 v98, v87, v98
	v_cvt_pk_f16_f32 v142, v82, v83
	v_cvt_pk_f16_f32 v143, v84, v85
	ds_read_b64_tr_b16 v[102:103], v207 offset:28672
	ds_read_b64_tr_b16 v[104:105], v207 offset:29696
	s_waitcnt lgkmcnt(14)
	v_mfma_f32_32x32x16_f16 v[50:65], v[166:169], v[138:141], v[50:65]
	v_add_f32_e32 v82, v88, v98
	v_add_f32_e32 v82, v89, v82
	v_add_f32_e32 v82, v90, v82
	v_add_f32_e32 v82, v91, v82
	v_cvt_pk_f16_f32 v144, v86, v87
	v_cvt_pk_f16_f32 v145, v88, v89
	ds_read_b64_tr_b16 v[98:99], v206 offset:30720
	ds_read_b64_tr_b16 v[100:101], v206 offset:31744
	s_waitcnt lgkmcnt(14)
	v_mfma_f32_32x32x16_f16 v[66:81], v[170:173], v[134:137], v[66:81]
	v_add_f32_e32 v82, v92, v82
	v_add_f32_e32 v82, v93, v82
	v_add_f32_e32 v82, v94, v82
	v_add_f32_e32 v82, v95, v82
	v_cvt_pk_f16_f32 v130, v90, v91
	v_cvt_pk_f16_f32 v131, v92, v93
	ds_read_b64_tr_b16 v[86:87], v207 offset:30720
	ds_read_b64_tr_b16 v[88:89], v207 offset:31744
	v_mfma_f32_32x32x16_f16 v[50:65], v[162:165], v[134:137], v[50:65]
	v_add_f32_e32 v82, v96, v82
	v_add_f32_e32 v84, v97, v82
	v_cvt_pk_f16_f32 v132, v94, v95
	v_cvt_pk_f16_f32 v133, v96, v97
	s_add_u32 s54, s50, 0x2000
	s_addc_u32 s55, s51, 0
	s_add_i32 s26, s39, s36
	s_mov_b32 m0, s26
	s_nop 0
	global_load_lds_dwordx4 v221, s[54:55]
	v_max_f32_e32 v82, v66, v67
	s_nop 1
	v_max3_f32 v83, v68, v69, v51
	v_max3_f32 v82, v82, v50, v52
	v_max3_f32 v82, v82, v53, v70
	v_max3_f32 v83, v83, v72, v73
	v_max3_f32 v82, v82, v71, v54
	v_max3_f32 v83, v83, v56, v57
	v_max3_f32 v82, v82, v55, v74
	v_max3_f32 v83, v83, v76, v77
	v_max3_f32 v82, v82, v75, v58
	v_max3_f32 v83, v83, v60, v61
	v_max3_f32 v82, v82, v59, v78
	v_max3_f32 v83, v83, v80, v81
	v_max3_f32 v82, v82, v79, v62
	v_max3_f32 v83, v83, v64, v65
	v_max3_f32 v82, v82, v63, v83
	v_mov_b32_e32 v83, v82
	v_add_f32_e32 v183, v198, v84
	s_nop 0
	v_permlane32_swap_b32_e32 v82, v83
	v_max_f32_e32 v82, v82, v83
	s_add_u32 s54, s52, 0x2000
	s_addc_u32 s55, s53, 0
	s_add_i32 s26, s43, s35
	s_mov_b32 m0, s26
	s_nop 0
	global_load_lds_dwordx4 v222, s[54:55]
	v_cmp_lt_f32_e32 vcc, s41, v82
	s_cmp_lg_u64 vcc, 0
	s_cselect_b64 s[26:27], -1, 0
	s_cbranch_vccnz .Lu1_12

.Lu2_1:
	ds_read_b64_tr_b16 v[178:179], v206 offset:32768
	ds_read_b64_tr_b16 v[180:181], v206 offset:33792
	s_waitcnt lgkmcnt(9)
	v_mfma_f32_32x32x16_f16 v[98:113], v[82:85], v[154:157], v[34:49]
	v_add_f32_e32 v86, v66, v67
	v_add_f32_e32 v86, v68, v86
	v_add_f32_e32 v86, v69, v86
	v_add_f32_e32 v86, v70, v86
	v_add_f32_e32 v86, v71, v86
	v_cvt_pk_f16_f32 v158, v66, v67
	v_cvt_pk_f16_f32 v159, v68, v69
	ds_read_b64_tr_b16 v[174:175], v207 offset:32768
	ds_read_b64_tr_b16 v[176:177], v207 offset:33792
	v_add_f32_e32 v66, v72, v86
	s_waitcnt lgkmcnt(10)
	v_mfma_f32_32x32x16_f16 v[82:97], v[170:173], v[154:157], v[34:49]
	v_add_f32_e32 v66, v73, v66
	v_add_f32_e32 v66, v74, v66
	v_add_f32_e32 v66, v75, v66
	v_cvt_pk_f16_f32 v160, v70, v71
	v_cvt_pk_f16_f32 v161, v72, v73
	ds_read_b64_tr_b16 v[170:171], v206 offset:34816
	ds_read_b64_tr_b16 v[172:173], v206 offset:35840
	s_waitcnt lgkmcnt(11)
	v_mfma_f32_32x32x16_f16 v[98:113], v[166:169], v[146:149], v[98:113]
	v_add_f32_e32 v66, v76, v66
	v_add_f32_e32 v66, v77, v66
	v_add_f32_e32 v66, v78, v66
	v_add_f32_e32 v66, v79, v66
	v_cvt_pk_f16_f32 v150, v74, v75
	v_cvt_pk_f16_f32 v151, v76, v77
	ds_read_b64_tr_b16 v[74:75], v207 offset:34816
	ds_read_b64_tr_b16 v[76:77], v207 offset:35840
	s_waitcnt lgkmcnt(12)
	v_mfma_f32_32x32x16_f16 v[82:97], v[162:165], v[146:149], v[82:97]
	v_add_f32_e32 v66, v80, v66
	v_add_f32_e32 v66, v81, v66
	v_add_f32_e32 v66, v50, v66
	v_add_f32_e32 v66, v51, v66
	v_cvt_pk_f16_f32 v152, v78, v79
	v_cvt_pk_f16_f32 v153, v80, v81
	ds_read_b64_tr_b16 v[70:71], v206 offset:36864
	ds_read_b64_tr_b16 v[72:73], v206 offset:37888
	s_waitcnt lgkmcnt(13)
	v_mfma_f32_32x32x16_f16 v[98:113], v[126:129], v[138:141], v[98:113]
	v_add_f32_e32 v66, v52, v66
	v_add_f32_e32 v66, v53, v66
	v_add_f32_e32 v66, v54, v66
	v_add_f32_e32 v78, v55, v66
	v_cvt_pk_f16_f32 v142, v50, v51
	v_cvt_pk_f16_f32 v143, v52, v53
	ds_read_b64_tr_b16 v[66:67], v207 offset:36864
	ds_read_b64_tr_b16 v[68:69], v207 offset:37888
	s_waitcnt lgkmcnt(14)
	v_mfma_f32_32x32x16_f16 v[82:97], v[122:125], v[138:141], v[82:97]
	v_add_f32_e32 v50, v56, v78
	v_add_f32_e32 v50, v57, v50
	v_add_f32_e32 v50, v58, v50
	v_add_f32_e32 v50, v59, v50
	v_cvt_pk_f16_f32 v144, v54, v55
	v_cvt_pk_f16_f32 v145, v56, v57
	ds_read_b64_tr_b16 v[54:55], v206 offset:38912
	ds_read_b64_tr_b16 v[56:57], v206 offset:39936
	s_waitcnt lgkmcnt(14)
	v_mfma_f32_32x32x16_f16 v[98:113], v[118:121], v[134:137], v[98:113]
	v_add_f32_e32 v50, v60, v50
	v_add_f32_e32 v50, v61, v50
	v_add_f32_e32 v50, v62, v50
	v_add_f32_e32 v78, v63, v50
	v_cvt_pk_f16_f32 v130, v58, v59
	v_cvt_pk_f16_f32 v131, v60, v61
	ds_read_b64_tr_b16 v[50:51], v207 offset:38912
	ds_read_b64_tr_b16 v[52:53], v207 offset:39936
	v_mfma_f32_32x32x16_f16 v[82:97], v[114:117], v[134:137], v[82:97]
	v_add_f32_e32 v58, v64, v78
	v_add_f32_e32 v60, v65, v58
	v_cvt_pk_f16_f32 v132, v62, v63
	v_cvt_pk_f16_f32 v133, v64, v65
	s_add_i32 s26, s42, s36
	s_mov_b32 m0, s26
	s_nop 0
	global_load_lds_dwordx4 v221, s[50:51]
	s_add_i32 s26, s39, s35
	s_mov_b32 m0, s26
	s_nop 0
	global_load_lds_dwordx4 v222, s[52:53]
	v_max_f32_e32 v58, v98, v99
	v_max3_f32 v59, v100, v101, v83
	v_max3_f32 v58, v58, v82, v84
	v_max3_f32 v58, v58, v85, v102
	v_max3_f32 v59, v59, v104, v105
	v_max3_f32 v58, v58, v103, v86
	v_max3_f32 v59, v59, v88, v89
	v_max3_f32 v58, v58, v87, v106
	v_max3_f32 v59, v59, v108, v109
	v_max3_f32 v58, v58, v107, v90
	v_max3_f32 v59, v59, v92, v93
	v_max3_f32 v58, v58, v91, v110
	v_max3_f32 v59, v59, v112, v113
	v_max3_f32 v58, v58, v111, v94
	v_max3_f32 v59, v59, v96, v97
	v_max3_f32 v58, v58, v95, v59
	v_mov_b32_e32 v59, v58
	v_add_f32_e32 v198, v183, v60
	s_nop 0
	v_permlane32_swap_b32_e32 v58, v59
	v_max_f32_e32 v58, v58, v59
	v_cmp_lt_f32_e32 vcc, s41, v58
	s_cmp_lg_u64 vcc, 0
	s_cselect_b64 s[26:27], -1, 0
	s_cbranch_vccnz .Lu2_9

.Lu2_4:
	s_add_i32 s26, s39, 0x2000
	s_cmpk_lg_i32 s39, 0x4000
	s_cselect_b32 s43, s26, 0
	ds_read_b64_tr_b16 v[126:127], v206 offset:40960
	ds_read_b64_tr_b16 v[128:129], v206 offset:41984
	s_waitcnt lgkmcnt(9)
	v_mfma_f32_32x32x16_f16 v[66:81], v[58:61], v[154:157], v[34:49]
	v_add_f32_e32 v50, v98, v99
	v_add_f32_e32 v50, v100, v50
	v_add_f32_e32 v50, v101, v50
	v_add_f32_e32 v50, v102, v50
	v_add_f32_e32 v50, v103, v50
	v_cvt_pk_f16_f32 v158, v98, v99
	v_cvt_pk_f16_f32 v159, v100, v101
	ds_read_b64_tr_b16 v[122:123], v207 offset:40960
	ds_read_b64_tr_b16 v[124:125], v207 offset:41984
	v_add_f32_e32 v50, v104, v50
	v_add_f32_e32 v50, v105, v50
	v_add_f32_e32 v50, v106, v50
	v_add_f32_e32 v98, v107, v50
	s_waitcnt lgkmcnt(10)
	v_mfma_f32_32x32x16_f16 v[50:65], v[114:117], v[154:157], v[34:49]
	v_cvt_pk_f16_f32 v160, v102, v103
	v_cvt_pk_f16_f32 v161, v104, v105
	ds_read_b64_tr_b16 v[118:119], v206 offset:43008
	ds_read_b64_tr_b16 v[120:121], v206 offset:44032
	s_waitcnt lgkmcnt(11)
	v_mfma_f32_32x32x16_f16 v[66:81], v[182:185], v[146:149], v[66:81]
	v_add_f32_e32 v98, v108, v98
	v_add_f32_e32 v98, v109, v98
	v_add_f32_e32 v98, v110, v98
	v_add_f32_e32 v98, v111, v98
	v_cvt_pk_f16_f32 v150, v106, v107
	v_cvt_pk_f16_f32 v151, v108, v109
	ds_read_b64_tr_b16 v[114:115], v207 offset:43008
	ds_read_b64_tr_b16 v[116:117], v207 offset:44032
	s_waitcnt lgkmcnt(12)
	v_mfma_f32_32x32x16_f16 v[50:65], v[174:177], v[146:149], v[50:65]
	v_add_f32_e32 v98, v112, v98
	v_add_f32_e32 v98, v113, v98
	v_add_f32_e32 v98, v82, v98
	v_add_f32_e32 v98, v83, v98
	v_cvt_pk_f16_f32 v152, v110, v111
	v_cvt_pk_f16_f32 v153, v112, v113
	ds_read_b64_tr_b16 v[106:107], v206 offset:45056
	ds_read_b64_tr_b16 v[108:109], v206 offset:46080
	s_waitcnt lgkmcnt(13)
	v_mfma_f32_32x32x16_f16 v[66:81], v[178:181], v[138:141], v[66:81]
	v_add_f32_e32 v98, v84, v98
	v_add_f32_e32 v98, v85, v98
	v_add_f32_e32 v98, v86, v98
	v_add_f32_e32 v98, v87, v98
	v_cvt_pk_f16_f32 v142, v82, v83
	v_cvt_pk_f16_f32 v143, v84, v85
	ds_read_b64_tr_b16 v[102:103], v207 offset:45056
	ds_read_b64_tr_b16 v[104:105], v207 offset:46080
	s_waitcnt lgkmcnt(14)
	v_mfma_f32_32x32x16_f16 v[50:65], v[166:169], v[138:141], v[50:65]
	v_add_f32_e32 v82, v88, v98
	v_add_f32_e32 v82, v89, v82
	v_add_f32_e32 v82, v90, v82
	v_add_f32_e32 v82, v91, v82
	v_cvt_pk_f16_f32 v144, v86, v87
	v_cvt_pk_f16_f32 v145, v88, v89
	ds_read_b64_tr_b16 v[98:99], v206 offset:47104
	ds_read_b64_tr_b16 v[100:101], v206 offset:48128
	s_waitcnt lgkmcnt(14)
	v_mfma_f32_32x32x16_f16 v[66:81], v[170:173], v[134:137], v[66:81]
	v_add_f32_e32 v82, v92, v82
	v_add_f32_e32 v82, v93, v82
	v_add_f32_e32 v82, v94, v82
	v_add_f32_e32 v82, v95, v82
	v_cvt_pk_f16_f32 v130, v90, v91
	v_cvt_pk_f16_f32 v131, v92, v93
	ds_read_b64_tr_b16 v[86:87], v207 offset:47104
	ds_read_b64_tr_b16 v[88:89], v207 offset:48128
	v_mfma_f32_32x32x16_f16 v[50:65], v[162:165], v[134:137], v[50:65]
	v_add_f32_e32 v82, v96, v82
	v_add_f32_e32 v84, v97, v82
	v_cvt_pk_f16_f32 v132, v94, v95
	v_cvt_pk_f16_f32 v133, v96, v97
	s_add_u32 s54, s50, 0x2000
	s_addc_u32 s55, s51, 0
	s_add_i32 s26, s39, s36
	s_mov_b32 m0, s26
	s_nop 0
	global_load_lds_dwordx4 v221, s[54:55]
	v_max_f32_e32 v82, v66, v67
	s_nop 1
	v_max3_f32 v83, v68, v69, v51
	v_max3_f32 v82, v82, v50, v52
	v_max3_f32 v82, v82, v53, v70
	v_max3_f32 v83, v83, v72, v73
	v_max3_f32 v82, v82, v71, v54
	v_max3_f32 v83, v83, v56, v57
	v_max3_f32 v82, v82, v55, v74
	v_max3_f32 v83, v83, v76, v77
	v_max3_f32 v82, v82, v75, v58
	v_max3_f32 v83, v83, v60, v61
	v_max3_f32 v82, v82, v59, v78
	v_max3_f32 v83, v83, v80, v81
	v_max3_f32 v82, v82, v79, v62
	v_max3_f32 v83, v83, v64, v65
	v_max3_f32 v82, v82, v63, v83
	v_mov_b32_e32 v83, v82
	v_add_f32_e32 v183, v198, v84
	s_nop 0
	v_permlane32_swap_b32_e32 v82, v83
	v_max_f32_e32 v82, v82, v83
	s_add_u32 s54, s52, 0x2000
	s_addc_u32 s55, s53, 0
	s_add_i32 s26, s43, s35
	s_mov_b32 m0, s26
	s_nop 0
	global_load_lds_dwordx4 v222, s[54:55]
	v_cmp_lt_f32_e32 vcc, s41, v82
	s_cmp_lg_u64 vcc, 0
	s_cselect_b64 s[26:27], -1, 0
	s_cbranch_vccnz .Lu2_12

.Lattn_unit2:
	s_load_dwordx4 s[4:7], s[0:1], 0x0
	s_lshr_b32 s0, s2, 2
	s_and_b32 s3, s2, 7
	s_and_b32 s0, s0, 8
	s_or_b32 s30, s0, s3
	s_lshr_b32 s18, s2, 6
	s_mov_b32 s19, 0
	s_lshl_b32 s0, s2, 5
	v_readfirstlane_b32 s16, v0
	s_and_b32 s12, s0, 0x300
	s_xor_b32 s12, s12, s91
	s_lshl_b64 s[8:9], s[18:19], 15
	s_lshl_b32 s0, s30, 11
	s_lshr_b32 s33, s16, 6
	s_or_b32 s8, s8, s0
	s_or_b32 s0, s8, s12
	s_lshl_b32 s31, s33, 5
	s_add_u32 s0, s0, s31
	s_addc_u32 s1, s9, 0
	s_lshl_b64 s[0:1], s[0:1], 7
	s_waitcnt lgkmcnt(0)
	s_add_u32 s0, s4, s0
	s_addc_u32 s1, s5, s1
	s_lshl_b64 s[10:11], s[8:9], 7
	v_bfe_u32 v190, v0, 3, 3
	s_add_u32 s10, s4, s10
	v_lshl_or_b32 v182, s33, 3, v190
	s_addc_u32 s11, s5, s11
	v_lshrrev_b32_e32 v89, 1, v182
	s_add_u32 s14, s10, 0x1000000
	v_xor_b32_e32 v4, v89, v0
	s_addc_u32 s15, s11, 0
	v_mov_b32_e32 v183, 0
	v_lshlrev_b32_e32 v4, 4, v4
	s_add_u32 s10, s10, 0x2000000
	v_lshlrev_b64 v[86:87], 7, v[182:183]
	v_and_b32_e32 v1, 7, v0
	v_and_b32_e32 v182, 0x70, v4
	v_lshrrev_b32_e32 v4, 2, v0
	s_addc_u32 s11, s11, 0
	v_lshl_add_u64 v[2:3], s[14:15], 0, v[86:87]
	v_bitop3_b32 v4, v4, v1, 4 bitop3:0x6c
	v_lshl_add_u64 v[186:187], v[2:3], 0, v[182:183]
	v_lshl_add_u64 v[2:3], s[10:11], 0, v[86:87]
	v_lshlrev_b32_e32 v182, 4, v4
	s_lshl_b32 s36, s33, 10
	s_mov_b64 s[20:21], 0x2000
	v_and_b32_e32 v191, 31, v0
	v_lshl_add_u64 v[194:195], v[2:3], 0, v[182:183]
	s_add_i32 s35, s36, 0x6000
	v_lshl_add_u64 v[2:3], v[186:187], 0, s[20:21]
	v_bfe_u32 v88, v0, 5, 1
	s_add_i32 s37, s36, 0x2000
	v_lshlrev_b32_e32 v2, 6, v191
	v_lshl_or_b32 v192, v88, 3, v2
	v_lshlrev_b32_e32 v14, 1, v192
	v_lshrrev_b32_e32 v18, 1, v0
	s_mov_b64 s[22:23], 0x4000
	v_mov_b32_e32 v2, v183
	v_mov_b32_e32 v3, v183
	v_mov_b32_e32 v4, v183
	v_mov_b32_e32 v5, v183
	v_mov_b32_e32 v6, v183
	v_mov_b32_e32 v7, v183
	v_mov_b32_e32 v8, v183
	v_mov_b32_e32 v9, v183
	v_mov_b32_e32 v10, v183
	v_mov_b32_e32 v11, v183
	v_mov_b32_e32 v12, v183
	v_mov_b32_e32 v13, v183
	v_mov_b32_e32 v14, v183
	v_mov_b32_e32 v15, v183
	v_mov_b32_e32 v16, v183
	v_mov_b32_e32 v17, v183
	v_lshlrev_b32_e32 v38, 7, v191
	v_bitop3_b32 v18, v88, v18, 7 bitop3:0x78
	v_lshl_or_b32 v211, v18, 4, v38
	v_lshl_add_u64 v[18:19], v[186:187], 0, s[22:23]
	s_add_i32 s0, s36, 0x4000
	s_waitcnt vmcnt(4) lgkmcnt(0)
	s_barrier
	ds_read_b128 v[34:37], v211
	v_bfe_u32 v39, v0, 1, 3
	v_bitop3_b32 v40, v88, v39, 2 bitop3:0x36
	v_lshl_or_b32 v210, v40, 4, v38
	v_bitop3_b32 v40, v88, v39, 4 bitop3:0x36
	v_lshl_or_b32 v209, v40, 4, v38
	v_bitop3_b32 v39, v88, v39, 6 bitop3:0x36
	v_lshl_or_b32 v208, v39, 4, v38
	v_lshlrev_b32_e32 v201, 9, v88
	s_and_b32 s0, s16, 0x3fffffc0
	s_mov_b64 s[24:25], 0x6000
	s_lshl_b32 s38, s0, 2
	s_add_i32 s34, s36, 0x8000
	s_lshl_b32 s2, s2, 16
	s_lshl_b32 s3, s3, 18
	s_waitcnt vmcnt(4) lgkmcnt(0)
	v_mfma_f32_32x32x16_f16 v[18:33], v[34:37], v[154:157], v[2:17]
	ds_read_b128 v[34:37], v211 offset:4096
	s_and_b32 s2, s2, 0x200000
	s_lshl_b64 s[16:17], s[18:19], 22
	s_or_b32 s2, s2, s3
	s_or_b32 s16, s16, s2
	s_mov_b64 s[2:3], 0x1002000
	v_and_b32_e32 v90, 63, v0
	s_waitcnt lgkmcnt(0)
	v_mfma_f32_32x32x16_f16 v[2:17], v[34:37], v[154:157], v[2:17]
	ds_read_b128 v[34:37], v210
	s_mov_b32 s13, s19
	s_movk_i32 s42, 0x2000
	s_movk_i32 s39, 0x4000
	v_lshl_or_b32 v204, v191, 2, s38
	v_lshlrev_b32_e32 v212, 4, v88
	s_mov_b32 s40, -1
	s_waitcnt vmcnt(4) lgkmcnt(0)
	v_mfma_f32_32x32x16_f16 v[18:33], v[34:37], v[146:149], v[18:33]
	ds_read_b128 v[34:37], v210 offset:4096
	s_mov_b32 s41, 0x41000000
	s_mov_b32 s26, s19
	s_waitcnt lgkmcnt(0)
	v_mfma_f32_32x32x16_f16 v[2:17], v[34:37], v[146:149], v[2:17]
	ds_read_b128 v[34:37], v209
	s_waitcnt vmcnt(4) lgkmcnt(0)
	v_mfma_f32_32x32x16_f16 v[18:33], v[34:37], v[138:141], v[18:33]
	ds_read_b128 v[34:37], v209 offset:4096
	ds_read_b128 v[38:41], v208 offset:4096
	ds_read_b128 v[42:45], v208
	s_waitcnt lgkmcnt(2)
	v_mfma_f32_32x32x16_f16 v[2:17], v[34:37], v[138:141], v[2:17]
	v_lshlrev_b32_e32 v34, 5, v0
	v_lshlrev_b32_e32 v35, 1, v0
	v_lshlrev_b32_e32 v36, 3, v0
	v_and_b32_e32 v34, 0x180, v34
	v_and_b32_e32 v193, 24, v36
	v_and_or_b32 v34, v35, 32, v34
	v_or3_b32 v203, v34, v193, v201
	s_waitcnt vmcnt(4) lgkmcnt(0)
	v_mfma_f32_32x32x16_f16 v[18:33], v[42:45], v[134:137], v[18:33]
	v_and_b32_e32 v200, 64, v36
	v_bitop3_b32 v202, v36, 64, v36 bitop3:0xc
	v_or_b32_e32 v206, v203, v200
	v_or_b32_e32 v207, v203, v202
	v_mfma_f32_32x32x16_f16 v[2:17], v[38:41], v[134:137], v[2:17]
	s_nop 15
	s_nop 7
	s_nop 0
	v_max3_f32 v34, v18, v19, v2
	v_max3_f32 v35, v20, v21, v3
	s_nop 0
	v_max3_f32 v34, v34, v4, v5
	v_max3_f32 v35, v35, v24, v25
	s_nop 0
	v_max3_f32 v34, v34, v22, v23
	v_max3_f32 v35, v35, v8, v9
	s_nop 0
	v_max3_f32 v34, v34, v6, v7
	v_max3_f32 v35, v35, v28, v29
	s_nop 0
	v_max3_f32 v34, v34, v26, v27
	v_max3_f32 v35, v35, v12, v13
	s_nop 0
	v_max3_f32 v34, v34, v10, v11
	v_max3_f32 v35, v35, v32, v33
	s_nop 0
	v_max3_f32 v34, v34, v30, v31
	v_max3_f32 v35, v35, v16, v17
	s_nop 0
	v_max3_f32 v34, v34, v14, v15
	s_nop 0
	v_max_f32_e32 v34, v34, v35
	s_nop 0
	v_mov_b32_e32 v35, v34
	s_nop 1
	v_permlane32_swap_b32_e32 v34, v35
	v_max_f32_e32 v34, v34, v35
	s_nop 0
	v_add_f32_e32 v205, v183, v34
	v_sub_f32_e32 v18, v18, v34
	v_sub_f32_e32 v2, v2, v34
	v_sub_f32_e32 v19, v19, v34
	v_sub_f32_e32 v3, v3, v34
	v_sub_f32_e32 v20, v20, v34
	v_sub_f32_e32 v4, v4, v34
	v_sub_f32_e32 v21, v21, v34
	v_sub_f32_e32 v5, v5, v34
	v_sub_f32_e32 v22, v22, v34
	v_sub_f32_e32 v6, v6, v34
	v_sub_f32_e32 v23, v23, v34
	v_sub_f32_e32 v7, v7, v34
	v_sub_f32_e32 v24, v24, v34
	v_sub_f32_e32 v8, v8, v34
	v_sub_f32_e32 v25, v25, v34
	v_sub_f32_e32 v9, v9, v34
	v_sub_f32_e32 v26, v26, v34
	v_sub_f32_e32 v10, v10, v34
	v_sub_f32_e32 v27, v27, v34
	v_sub_f32_e32 v11, v11, v34
	v_sub_f32_e32 v28, v28, v34
	v_sub_f32_e32 v12, v12, v34
	v_sub_f32_e32 v29, v29, v34
	v_sub_f32_e32 v13, v13, v34
	v_sub_f32_e32 v30, v30, v34
	v_sub_f32_e32 v14, v14, v34
	v_sub_f32_e32 v31, v31, v34
	v_sub_f32_e32 v15, v15, v34
	v_sub_f32_e32 v32, v32, v34
	v_sub_f32_e32 v16, v16, v34
	v_sub_f32_e32 v33, v33, v34
	v_sub_f32_e32 v17, v17, v34
	s_nop 0
	v_xor_b32_e32 v34, 0x80000000, v205
	v_mov_b32_e32 v35, v34
	v_mov_b32_e32 v36, v34
	v_mov_b32_e32 v37, v34
	v_mov_b32_e32 v38, v34
	v_mov_b32_e32 v39, v34
	v_mov_b32_e32 v40, v34
	v_mov_b32_e32 v41, v34
	v_mov_b32_e32 v42, v34
	v_mov_b32_e32 v43, v34
	v_mov_b32_e32 v44, v34
	v_mov_b32_e32 v45, v34
	v_mov_b32_e32 v46, v34
	v_mov_b32_e32 v47, v34
	v_mov_b32_e32 v48, v34
	v_mov_b32_e32 v49, v34
	s_waitcnt vmcnt(0) lgkmcnt(0)
	s_barrier
	v_exp_f32_e32 v50, v2
	v_exp_f32_e32 v51, v3
	v_lshl_add_u64 v[2:3], v[186:187], 0, s[24:25]
	s_mov_b32 s0, m0
	s_mov_b32 m0, s36
	s_nop 0
	global_load_lds_dwordx4 v[2:3], off
	s_mov_b32 m0, s0
	v_lshl_add_u64 v[2:3], v[194:195], 0, s[20:21]
	s_mov_b32 s0, m0
	s_mov_b32 m0, s34
	s_nop 0
	global_load_lds_dwordx4 v[2:3], off
	s_mov_b32 m0, s0
	ds_read_b128 v[82:85], v211 offset:8192
	ds_read_b128 v[170:173], v211 offset:12288
	ds_read_b128 v[166:169], v210 offset:8192
	ds_read_b128 v[162:165], v210 offset:12288
	ds_read_b128 v[126:129], v209 offset:8192
	ds_read_b128 v[122:125], v209 offset:12288
	ds_read_b128 v[118:121], v208 offset:8192
	ds_read_b128 v[114:117], v208 offset:12288
	v_exp_f32_e32 v52, v4
	v_lshl_add_u64 v[2:3], s[16:17], 0, v[86:87]
	v_bitop3_b32 v4, v89, 7, v0 bitop3:0x48
	v_exp_f32_e32 v66, v18
	v_exp_f32_e32 v67, v19
	v_exp_f32_e32 v68, v20
	v_exp_f32_e32 v69, v21
	v_exp_f32_e32 v70, v22
	v_exp_f32_e32 v71, v23
	v_exp_f32_e32 v72, v24
	v_exp_f32_e32 v73, v25
	v_exp_f32_e32 v74, v26
	v_exp_f32_e32 v75, v27
	v_exp_f32_e32 v76, v28
	v_exp_f32_e32 v77, v29
	v_exp_f32_e32 v78, v30
	v_exp_f32_e32 v79, v31
	v_exp_f32_e32 v80, v32
	v_exp_f32_e32 v81, v33
	v_exp_f32_e32 v53, v5
	v_exp_f32_e32 v54, v6
	v_exp_f32_e32 v55, v7
	v_exp_f32_e32 v56, v8
	v_exp_f32_e32 v57, v9
	v_exp_f32_e32 v58, v10
	v_exp_f32_e32 v59, v11
	v_exp_f32_e32 v60, v12
	v_exp_f32_e32 v61, v13
	v_exp_f32_e32 v62, v14
	v_exp_f32_e32 v63, v15
	v_exp_f32_e32 v64, v16
	v_exp_f32_e32 v65, v17
	v_lshl_or_b32 v4, v4, 4, v2
	v_mov_b32_e32 v5, v3
	s_waitcnt vmcnt(2) lgkmcnt(0)
	s_barrier
	v_lshl_add_u64 v[4:5], s[4:5], 0, v[4:5]
	v_or_b32_e32 v2, v2, v182
	v_lshl_add_u64 v[188:189], v[4:5], 0, s[2:3]
	v_lshl_add_u64 v[2:3], s[4:5], 0, v[2:3]
	s_mov_b64 s[2:3], 0x2002000
	v_cmp_gt_u32_e64 s[0:1], 32, v90
	v_lshl_add_u64 v[196:197], v[2:3], 0, s[2:3]
	s_mov_b64 s[2:3], 0x8000
	v_mov_b32_e32 v2, v183
	v_mov_b32_e32 v3, v183
	v_mov_b32_e32 v4, v183
	v_mov_b32_e32 v5, v183
	v_mov_b32_e32 v6, v183
	v_mov_b32_e32 v7, v183
	v_mov_b32_e32 v8, v183
	v_mov_b32_e32 v9, v183
	v_mov_b32_e32 v10, v183
	v_mov_b32_e32 v11, v183
	v_mov_b32_e32 v12, v183
	v_mov_b32_e32 v13, v183
	v_mov_b32_e32 v14, v183
	v_mov_b32_e32 v15, v183
	v_mov_b32_e32 v16, v183
	v_mov_b32_e32 v17, v183
	v_mov_b32_e32 v18, v183
	v_mov_b32_e32 v19, v183
	v_mov_b32_e32 v20, v183
	v_mov_b32_e32 v21, v183
	v_mov_b32_e32 v22, v183
	v_mov_b32_e32 v23, v183
	v_mov_b32_e32 v24, v183
	v_mov_b32_e32 v25, v183
	v_mov_b32_e32 v26, v183
	v_mov_b32_e32 v27, v183
	v_mov_b32_e32 v28, v183
	v_mov_b32_e32 v29, v183
	v_mov_b32_e32 v30, v183
	v_mov_b32_e32 v31, v183
	v_mov_b32_e32 v32, v183
	v_mov_b32_e32 v33, v183
	v_subrev_u32_e32 v221, s14, v186
	v_subrev_u32_e32 v222, s10, v194
	s_add_u32 s50, s14, 0x8000
	s_addc_u32 s51, s15, 0
	s_add_u32 s52, s10, 0x4000
	s_addc_u32 s53, s11, 0
	s_branch .Lu0_1
